# baseline (speedup 1.0000x reference)
_Z14seg_sum_kernelPKfS0_S0_PDv8_DF16bS2_Pf:
	s_ashr_i32 s4, s2, 2
	s_load_dwordx4 s[12:15], s[0:1], 0x0
	s_and_b32 s3, s2, 7
	s_and_b32 s4, s4, -8
	s_or_b32 s3, s4, s3
	v_readfirstlane_b32 s5, v0
	s_ashr_i32 s4, s3, 2
	s_lshr_b32 s11, s5, 6
	s_mul_hi_u32 s5, s5, 0xaaaaaaab
	s_lshr_b32 s23, s5, 7
	s_ashr_i32 s5, s4, 31
	s_and_b32 s22, s2, 3
	s_lshl_b64 s[6:7], s[4:5], 19
	s_waitcnt lgkmcnt(0)
	s_add_u32 s5, s14, s6
	s_addc_u32 s6, s15, s7
	s_lshl_b32 s14, s22, 10
	s_lshl_b32 s8, s22, 12
	s_add_u32 s8, s5, s8
	v_lshlrev_b32_e32 v2, 6, v0
	v_add_u32_e32 v122, 0x300, v0
	s_addc_u32 s9, s6, 0
	v_lshlrev_b32_e32 v1, 4, v0
	v_and_b32_e32 v2, 0xc000, v2
	v_mov_b32_e32 v3, 0
	v_lshlrev_b32_e32 v6, 6, v122
	v_lshl_add_u64 v[4:5], s[8:9], 0, v[2:3]
	v_and_b32_e32 v2, 0xff0, v1
	v_lshlrev_b32_e32 v1, 4, v122
	v_and_b32_e32 v6, 0x1c000, v6
	v_mov_b32_e32 v7, v3
	v_lshl_add_u64 v[4:5], v[4:5], 0, v[2:3]
	v_lshl_add_u64 v[6:7], s[8:9], 0, v[6:7]
	v_and_b32_e32 v8, 0xff0, v1
	v_mov_b32_e32 v9, v3
	v_add_u32_e32 v123, 0x600, v0
	v_lshl_add_u64 v[6:7], v[6:7], 0, v[8:9]
	global_load_dwordx4 v[82:85], v[4:5], off
	global_load_dwordx4 v[78:81], v[6:7], off
	v_lshlrev_b32_e32 v4, 6, v123
	v_lshlrev_b32_e32 v1, 4, v123
	v_and_b32_e32 v4, 0x3c000, v4
	v_mov_b32_e32 v5, v3
	v_lshl_add_u64 v[4:5], s[8:9], 0, v[4:5]
	v_and_b32_e32 v6, 0xff0, v1
	v_mov_b32_e32 v7, v3
	v_add_u32_e32 v124, 0x900, v0
	v_lshl_add_u64 v[4:5], v[4:5], 0, v[6:7]
	v_lshlrev_b32_e32 v6, 6, v124
	v_lshlrev_b32_e32 v1, 4, v124
	v_and_b32_e32 v6, 0x3c000, v6
	v_lshl_add_u64 v[6:7], s[8:9], 0, v[6:7]
	v_and_b32_e32 v8, 0xff0, v1
	v_or_b32_e32 v125, 0xc00, v0
	v_lshl_add_u64 v[6:7], v[6:7], 0, v[8:9]
	v_lshlrev_b32_e32 v1, 6, v125
	v_add_u32_e32 v130, 0xf00, v0
	global_load_dwordx4 v[90:93], v[4:5], off
	global_load_dwordx4 v[86:89], v[6:7], off
	v_and_b32_e32 v4, 0x3c000, v1
	v_mov_b32_e32 v5, v3
	v_lshlrev_b32_e32 v6, 6, v130
	v_lshl_add_u64 v[4:5], s[8:9], 0, v[4:5]
	v_lshlrev_b32_e32 v1, 4, v130
	v_and_b32_e32 v6, 0x7c000, v6
	v_mov_b32_e32 v7, v3
	v_lshl_add_u64 v[4:5], v[4:5], 0, v[2:3]
	v_lshl_add_u64 v[6:7], s[8:9], 0, v[6:7]
	v_and_b32_e32 v8, 0xff0, v1
	v_add_u32_e32 v131, 0x1200, v0
	v_lshl_add_u64 v[6:7], v[6:7], 0, v[8:9]
	global_load_dwordx4 v[98:101], v[4:5], off
	global_load_dwordx4 v[94:97], v[6:7], off
	v_lshlrev_b32_e32 v4, 6, v131
	v_lshlrev_b32_e32 v1, 4, v131
	v_and_b32_e32 v4, 0x5c000, v4
	v_mov_b32_e32 v5, v3
	v_lshl_add_u64 v[4:5], s[8:9], 0, v[4:5]
	v_and_b32_e32 v6, 0xff0, v1
	v_mov_b32_e32 v7, v3
	v_add_u32_e32 v134, 0x1500, v0
	v_lshl_add_u64 v[4:5], v[4:5], 0, v[6:7]
	v_lshlrev_b32_e32 v6, 6, v134
	v_lshlrev_b32_e32 v1, 4, v134
	v_and_b32_e32 v6, 0x7c000, v6
	v_or_b32_e32 v135, 0x1800, v0
	v_lshl_add_u64 v[6:7], s[8:9], 0, v[6:7]
	v_and_b32_e32 v8, 0xff0, v1
	v_lshlrev_b32_e32 v1, 6, v135
	v_lshl_add_u64 v[6:7], v[6:7], 0, v[8:9]
	global_load_dwordx4 v[106:109], v[4:5], off
	global_load_dwordx4 v[102:105], v[6:7], off
	v_and_b32_e32 v4, 0x6c000, v1
	v_mov_b32_e32 v5, v3
	v_lshl_add_u64 v[4:5], s[8:9], 0, v[4:5]
	v_add_u32_e32 v136, 0x1b00, v0
	v_lshl_add_u64 v[4:5], v[4:5], 0, v[2:3]
	v_lshlrev_b32_e32 v2, 6, v136
	v_lshlrev_b32_e32 v1, 4, v136
	v_and_b32_e32 v2, 0x7c000, v2
	v_lshl_add_u64 v[6:7], s[8:9], 0, v[2:3]
	v_and_b32_e32 v2, 0xff0, v1
	v_add_u32_e32 v137, 0x1e00, v0
	v_lshl_add_u64 v[6:7], v[6:7], 0, v[2:3]
	v_min_u32_e32 v1, 0x1fff, v137
	global_load_dwordx4 v[118:121], v[4:5], off
	global_load_dwordx4 v[110:113], v[6:7], off
	v_lshlrev_b32_e32 v6, 4, v1
	v_lshlrev_b32_e32 v1, 6, v1
	v_and_b32_e32 v2, 0x7c000, v1
	v_bfe_u32 v127, v0, 4, 2
	s_lshl_b32 s4, s4, 12
	v_lshl_add_u64 v[4:5], s[8:9], 0, v[2:3]
	v_and_b32_e32 v2, 0xff0, v6
	v_lshlrev_b32_e32 v133, 3, v127
	s_or_b32 s4, s14, s4
	v_lshl_add_u64 v[4:5], v[4:5], 0, v[2:3]
	s_lshl_b32 s26, s23, 8
	v_or_b32_e32 v2, s4, v133
	s_movk_i32 s10, 0xc00
	global_load_dwordx4 v[114:117], v[4:5], off
	s_mul_hi_u32 s6, s11, 0x55555556
	v_add_u32_e32 v28, s26, v2
	v_mov_b64_e32 v[4:5], s[12:13]
	s_mov_b32 s7, 0
	s_bfe_u32 s24, s2, 0x20003
	s_mul_i32 s6, s6, 3
	v_mad_i64_i32 v[4:5], s[8:9], v28, s10, v[4:5]
	s_sub_i32 s25, s11, s6
	s_mul_i32 s8, s24, 0x300
	s_mov_b32 s9, s7
	v_and_b32_e32 v1, 15, v0
	v_lshl_add_u64 v[4:5], v[4:5], 0, s[8:9]
	s_lshl_b32 s8, s25, 8
	v_lshl_add_u64 v[4:5], v[4:5], 0, s[8:9]
	v_lshlrev_b32_e32 v2, 4, v1
	v_lshl_add_u64 v[4:5], v[4:5], 0, v[2:3]
	s_movk_i32 s4, 0x1000
	v_add_co_u32_e32 v6, vcc, s4, v4
	s_movk_i32 s4, 0x2000
	s_nop 0
	v_addc_co_u32_e32 v7, vcc, 0, v5, vcc
	v_add_co_u32_e32 v8, vcc, s4, v4
	s_movk_i32 s4, 0x3000
	s_nop 0
	v_addc_co_u32_e32 v9, vcc, 0, v5, vcc
	global_load_dwordx4 v[18:21], v[4:5], off nt
	global_load_dwordx4 v[30:33], v[4:5], off offset:3072 nt
	global_load_dwordx4 v[46:49], v[6:7], off offset:2048 nt
	global_load_dwordx4 v[50:53], v[8:9], off offset:1024 nt
	v_add_co_u32_e32 v6, vcc, s4, v4
	s_movk_i32 s4, 0x4000
	s_nop 0
	v_addc_co_u32_e32 v7, vcc, 0, v5, vcc
	global_load_dwordx4 v[62:65], v[6:7], off nt
	global_load_dwordx4 v[66:69], v[6:7], off offset:3072 nt
	v_add_co_u32_e32 v6, vcc, s4, v4
	s_movk_i32 s4, 0x5000
	s_nop 0
	v_addc_co_u32_e32 v7, vcc, 0, v5, vcc
	v_add_co_u32_e32 v8, vcc, s4, v4
	s_mov_b32 s4, 0x18000
	s_nop 0
	v_addc_co_u32_e32 v9, vcc, 0, v5, vcc
	v_add_co_u32_e32 v10, vcc, s4, v4
	s_mov_b32 s4, 0x19000
	s_nop 0
	v_addc_co_u32_e32 v11, vcc, 0, v5, vcc
	v_add_co_u32_e32 v14, vcc, s4, v4
	s_mov_b32 s4, 0x1a000
	s_nop 0
	v_addc_co_u32_e32 v15, vcc, 0, v5, vcc
	v_add_co_u32_e32 v22, vcc, s4, v4
	s_mov_b32 s4, 0x1b000
	s_nop 0
	v_addc_co_u32_e32 v23, vcc, 0, v5, vcc
	v_add_co_u32_e32 v26, vcc, s4, v4
	s_mov_b32 s5, 0x1c000
	s_nop 0
	v_addc_co_u32_e32 v27, vcc, 0, v5, vcc
	global_load_dwordx4 v[70:73], v[6:7], off offset:2048 nt
	global_load_dwordx4 v[74:77], v[8:9], off offset:1024 nt
	s_nop 0
	global_load_dwordx4 v[6:9], v[10:11], off nt
	s_nop 0
	global_load_dwordx4 v[10:13], v[10:11], off offset:3072 nt
	s_nop 0
	global_load_dwordx4 v[14:17], v[14:15], off offset:2048 nt
	s_nop 0
	global_load_dwordx4 v[22:25], v[22:23], off offset:1024 nt
	s_nop 0
	global_load_dwordx4 v[38:41], v[26:27], off nt
	global_load_dwordx4 v[42:45], v[26:27], off offset:3072 nt
	v_add_co_u32_e32 v26, vcc, s5, v4
	s_mov_b32 s4, 0x1d000
	s_nop 0
	v_addc_co_u32_e32 v27, vcc, 0, v5, vcc
	v_add_co_u32_e32 v4, vcc, s4, v4
	v_lshrrev_b32_e32 v126, 3, v0
	s_nop 0
	v_addc_co_u32_e32 v5, vcc, 0, v5, vcc
	global_load_dwordx4 v[54:57], v[26:27], off offset:2048 nt
	global_load_dwordx4 v[58:61], v[4:5], off offset:1024 nt
	v_mad_i64_i32 v[4:5], s[4:5], v28, s10, 0
	s_lshl_b32 s4, s2, 1
	s_nop 0
	v_bfi_b32 v132, -8, s4, v0
	v_mad_u64_u32 v[128:129], s[4:5], s22, 24, v[126:127]
	s_movk_i32 s4, 0xc0
	s_lshl_b32 s6, s25, 6
	v_cmp_gt_u32_e64 s[4:5], s4, v0
	v_mov_b32_e32 v26, v3
	v_mov_b32_e32 v27, v3
	v_mov_b32_e32 v28, v3
	v_mov_b32_e32 v29, v3
	v_mov_b32_e32 v34, v3
	v_mov_b32_e32 v35, v3
	v_mov_b32_e32 v36, v3
	v_mov_b32_e32 v37, v3
	s_and_saveexec_b64 s[8:9], s[4:5]
	s_cbranch_execz .LBB0_2
	s_load_dwordx2 s[14:15], s[0:1], 0x10
	v_lshlrev_b32_e32 v26, 5, v128
	v_mov_b32_e32 v27, 0
	s_waitcnt lgkmcnt(0)
	v_mov_b64_e32 v[28:29], s[14:15]
	v_mad_i64_i32 v[28:29], s[10:11], v132, s10, v[28:29]
	v_lshl_add_u64 v[34:35], v[28:29], 0, v[26:27]
	global_load_dwordx4 v[26:29], v[34:35], off offset:16
	s_nop 0
	global_load_dwordx4 v[34:37], v[34:35], off
